# row loops NORM_A, NORM_B, NORM_C: next-row loads kept in flight during compute (re-measure 1)
# baseline (speedup 1.0000x reference)
_Z6mk_fwd4Args:
	s_mov_b32 s98, 0
	s_mov_b32 s6, s2
	s_mov_b64 s[2:3], s[0:1]
	s_load_dwordx2 s[86:87], s[0:1], 0xa8
	s_nop 0
	s_load_dword s0, s[0:1], 0xb8
	v_readfirstlane_b32 s24, v0
	s_waitcnt lgkmcnt(0)
	v_writelane_b32 v254, s0, 0
	s_add_u32 s0, s2, 0xb8
	v_writelane_b32 v254, s2, 1
	s_addc_u32 s1, s3, 0
	s_nop 0
	v_writelane_b32 v254, s3, 2
	v_writelane_b32 v254, s0, 3
	v_cmp_gt_u32_e64 s[2:3], 64, v0
	s_nop 0
	v_writelane_b32 v254, s1, 4
	v_cmp_lt_u32_e64 s[0:1], 63, v0
	s_nop 1
	v_writelane_b32 v254, s0, 5
	s_nop 1
	v_writelane_b32 v254, s1, 6
	s_mov_b64 s[0:1], exec
	v_writelane_b32 v254, s2, 7
	s_nop 1
	v_writelane_b32 v254, s3, 8
	s_and_b64 s[2:3], s[0:1], s[2:3]
	s_mov_b64 exec, s[2:3]
	v_lshl_add_u32 v1, v0, 2, 0
	v_add_u32_e32 v1, 0x25f00, v1
	v_mov_b32_e32 v2, 0
	ds_write_b32 v1, v2
	s_or_b64 exec, exec, s[0:1]
	s_add_u32 s0, s86, 0x4000
	s_addc_u32 s1, s87, 0
	v_writelane_b32 v254, s0, 9
	s_waitcnt lgkmcnt(0)
	s_barrier
	v_writelane_b32 v254, s1, 10
	s_getreg_b32 s0, hwreg(HW_REG_XCC_ID, 0, 4)
	s_and_b32 s0, s0, 15
	v_writelane_b32 v254, s0, 11
	v_cmp_eq_u32_e64 s[2:3], 0, v0
	s_mov_b64 s[0:1], exec
	s_nop 0
	v_writelane_b32 v254, s2, 12
	s_nop 1
	v_writelane_b32 v254, s3, 13
	s_and_b64 s[2:3], s[0:1], s[2:3]
	s_mov_b64 exec, s[2:3]
	s_cbranch_execz .LBB0_5
	s_mov_b64 s[2:3], exec
	v_mbcnt_lo_u32_b32 v1, s2, 0
	v_mbcnt_hi_u32_b32 v1, s3, v1
	v_cmp_eq_u32_e32 vcc, 0, v1
	s_and_b64 s[4:5], exec, vcc
	s_mov_b64 exec, s[4:5]
	s_cbranch_execz .LBB0_5
	v_readlane_b32 s4, v254, 11
	s_bcnt1_i32_b64 s2, s[2:3]
	s_lshl_b32 s4, s4, 8
	v_mov_b32_e32 v2, s2
	v_readlane_b32 s2, v254, 9
	v_mov_b32_e32 v1, s4
	v_readlane_b32 s3, v254, 10
	s_nop 4
	global_atomic_add v1, v2, s[2:3] offset:1024

.LBB0_1469:
	s_add_i32 s98, s98, 1
	s_cmp_lt_u32 s98, 5
	s_cbranch_scc0 .Lprobe_cont
	s_mov_b64 s[0:1], -1
	s_mov_b64 s[4:5], -1
	s_branch .LBB0_1407
.Lprobe_cont:
	s_mov_b32 s98, 0
	s_cmp_lt_i32 s78, 10
	s_cselect_b64 s[4:5], -1, 0
	s_add_u32 s20, s86, 0x5b200000
	s_addc_u32 s21, s87, 0
	s_and_b64 s[0:1], s[4:5], s[0:1]
	s_andn2_b64 vcc, exec, s[0:1]
	s_cbranch_vccnz .LBB0_1486
	v_readlane_b32 s4, v254, 14
	s_cmpk_gt_i32 s4, 0x15ff
	v_readfirstlane_b32 s12, v0
	s_cbranch_scc1 .LBB0_1486
	v_lshrrev_b32_e32 v1, 5, v0
	v_lshrrev_b32_e32 v3, 1, v0
	v_and_b32_e32 v1, 4, v1
	v_bfe_u32 v2, v0, 2, 2
	v_and_b32_e32 v13, 24, v3
	v_or3_b32 v1, v1, v2, v13
	v_lshlrev_b32_e32 v2, 4, v0
	v_or_b32_e32 v10, 0x2000, v2
	s_add_u32 s15, s86, 0x2500000
	v_lshrrev_b32_e32 v3, 7, v10
	s_movk_i32 s4, 0x60
	v_readlane_b32 s6, v254, 14
	s_addc_u32 s33, s87, 0
	v_and_or_b32 v4, v3, s4, v1
	v_bfe_u32 v14, v0, 2, 4
	s_movk_i32 s4, 0x70
	s_ashr_i32 s37, s6, 31
	v_and_or_b32 v3, v3, s4, v14
	s_lshr_b32 s4, s37, 29
	s_add_i32 s4, s6, s4
	s_lshr_b32 s10, s12, 6
	s_ashr_i32 s5, s4, 3
	s_and_b32 s4, s4, -8
	s_lshr_b32 s9, s12, 8
	s_lshl_b32 s36, s10, 10
	s_sub_i32 s4, s6, s4
	s_cmp_lt_i32 s4, 0
	s_movk_i32 s38, 0x2c1
	s_cselect_b32 s6, s38, 0x2c0
	s_mul_i32 s4, s4, s6
	s_add_i32 s4, s4, s5
	s_mul_hi_i32 s5, s4, 0x2e8ba2e9
	s_lshr_b32 s6, s5, 31
	s_ashr_i32 s5, s5, 6
	s_add_i32 s5, s5, s6
	s_lshl_b32 s6, s5, 3
	s_mulk_i32 s5, 0x160
	s_sub_i32 s4, s4, s5
	s_sext_i32_i16 s5, s4
	s_bfe_u32 s5, s5, 0x3001c
	s_add_i32 s5, s4, s5
	s_sext_i32_i16 s7, s5
	s_and_b32 s5, s5, 0xfff8
	s_sub_i32 s4, s4, s5
	s_sext_i32_i16 s4, s4
	v_and_b32_e32 v5, 32, v0
	s_lshr_b32 s8, s7, 3
	s_add_i32 s26, s6, s4
	v_bitop3_b32 v11, v2, v5, 48 bitop3:0x6c
	v_and_b32_e32 v12, 64, v0
	s_ashr_i32 s27, s26, 31
	s_bfe_i64 s[6:7], s[8:9], 0x100000
	v_or_b32_e32 v2, v11, v12
	s_lshl_b64 s[4:5], s[26:27], 20
	s_lshl_b64 s[6:7], s[6:7], 20
	v_lshl_or_b32 v132, v3, 12, v2
	v_lshrrev_b32_e32 v3, 3, v0
	s_add_u32 s30, s15, s6
	v_and_or_b32 v1, v3, 32, v1
	s_addc_u32 s31, s33, s7
	s_add_i32 s39, s36, 0
	v_lshl_or_b32 v134, v1, 12, v2
	s_add_i32 m0, s39, 0x10000
	v_lshl_or_b32 v130, v4, 12, v2
	global_load_lds_dwordx4 v134, s[30:31]
	s_add_i32 m0, s39, 0x12000
	s_add_u32 s6, s30, 0x80000
	global_load_lds_dwordx4 v130, s[30:31]
	s_addc_u32 s7, s31, 0
	s_add_i32 m0, s39, 0x14000
	v_and_or_b32 v1, v3, 48, v14
	global_load_lds_dwordx4 v134, s[6:7]
	s_add_i32 m0, s39, 0x16000
	s_add_u32 s28, s20, s4
	s_addc_u32 s29, s21, s5
	s_add_i32 s40, s39, 0x2000
	v_lshl_or_b32 v136, v1, 12, v2
	global_load_lds_dwordx4 v130, s[6:7]
	s_mov_b32 m0, s39
	s_add_u32 s4, s28, 0x80000
	global_load_lds_dwordx4 v136, s[28:29]
	s_mov_b32 m0, s40
	s_addc_u32 s5, s29, 0
	s_add_i32 s41, s39, 0x4000
	global_load_lds_dwordx4 v132, s[28:29]
	s_mov_b32 m0, s41
	s_add_i32 s42, s39, 0x6000
	global_load_lds_dwordx4 v136, s[4:5]
	s_mov_b32 m0, s42
	v_mov_b32_e32 v135, 0
	global_load_lds_dwordx4 v132, s[4:5]
	v_mov_b32_e32 v131, v135
	v_mov_b32_e32 v137, v135
	v_mov_b32_e32 v133, v135
	s_cmp_eq_u32 s9, 1
	s_mov_b32 s43, 0
	v_lshl_add_u64 v[8:9], s[30:31], 0, v[134:135]
	v_lshl_add_u64 v[6:7], s[30:31], 0, v[130:131]
	v_lshl_add_u64 v[2:3], s[28:29], 0, v[136:137]
	s_cselect_b64 s[4:5], -1, 0
	s_cmp_lg_u32 s9, 1
	v_lshl_add_u64 v[4:5], s[28:29], 0, v[132:133]
	s_cbranch_scc1 .LBB0_1473
	s_barrier

	.amdhsa_kernel _Z6mk_fwd4Args
		.amdhsa_group_segment_fixed_size 0
		.amdhsa_private_segment_fixed_size 0
		.amdhsa_kernarg_size 440
		.amdhsa_user_sgpr_count 2
		.amdhsa_user_sgpr_dispatch_ptr 0
		.amdhsa_user_sgpr_queue_ptr 0
		.amdhsa_user_sgpr_kernarg_segment_ptr 1
		.amdhsa_user_sgpr_dispatch_id 0
		.amdhsa_user_sgpr_kernarg_preload_length 0
		.amdhsa_user_sgpr_kernarg_preload_offset 0
		.amdhsa_user_sgpr_private_segment_size 0
		.amdhsa_uses_dynamic_stack 0
		.amdhsa_enable_private_segment 0
		.amdhsa_system_sgpr_workgroup_id_x 1
		.amdhsa_system_sgpr_workgroup_id_y 0
		.amdhsa_system_sgpr_workgroup_id_z 0
		.amdhsa_system_sgpr_workgroup_info 0
		.amdhsa_system_vgpr_workitem_id 0
		.amdhsa_next_free_vgpr 256
		.amdhsa_next_free_sgpr 102
		.amdhsa_accum_offset 256
		.amdhsa_reserve_vcc 1
		.amdhsa_float_round_mode_32 0
		.amdhsa_float_round_mode_16_64 0
		.amdhsa_float_denorm_mode_32 3
		.amdhsa_float_denorm_mode_16_64 3
		.amdhsa_dx10_clamp 1
		.amdhsa_ieee_mode 1
		.amdhsa_fp16_overflow 0
		.amdhsa_tg_split 0
		.amdhsa_exception_fp_ieee_invalid_op 0
		.amdhsa_exception_fp_denorm_src 0
		.amdhsa_exception_fp_ieee_div_zero 0
		.amdhsa_exception_fp_ieee_overflow 0
		.amdhsa_exception_fp_ieee_underflow 0
		.amdhsa_exception_fp_ieee_inexact 0
		.amdhsa_exception_int_div_zero 0
	.end_amdhsa_kernel

amdhsa.kernels:
  - .agpr_count:     0
    .args:
      - .offset:         0
        .size:           184
        .value_kind:     by_value
      - .offset:         184
        .size:           4
        .value_kind:     hidden_block_count_x
      - .offset:         188
        .size:           4
        .value_kind:     hidden_block_count_y
      - .offset:         192
        .size:           4
        .value_kind:     hidden_block_count_z
      - .offset:         196
        .size:           2
        .value_kind:     hidden_group_size_x
      - .offset:         198
        .size:           2
        .value_kind:     hidden_group_size_y
      - .offset:         200
        .size:           2
        .value_kind:     hidden_group_size_z
      - .offset:         202
        .size:           2
        .value_kind:     hidden_remainder_x
      - .offset:         204
        .size:           2
        .value_kind:     hidden_remainder_y
      - .offset:         206
        .size:           2
        .value_kind:     hidden_remainder_z
      - .offset:         224
        .size:           8
        .value_kind:     hidden_global_offset_x
      - .offset:         232
        .size:           8
        .value_kind:     hidden_global_offset_y
      - .offset:         240
        .size:           8
        .value_kind:     hidden_global_offset_z
      - .offset:         248
        .size:           2
        .value_kind:     hidden_grid_dims
      - .offset:         304
        .size:           4
        .value_kind:     hidden_dynamic_lds_size
    .group_segment_fixed_size: 0
    .kernarg_segment_align: 8
    .kernarg_segment_size: 440
    .language:       OpenCL C
    .language_version:
      - 2
      - 0
    .max_flat_workgroup_size: 512
    .name:           _Z6mk_fwd4Args
    .private_segment_fixed_size: 0
    .sgpr_count:     108
    .sgpr_spill_count: 96
    .symbol:         _Z6mk_fwd4Args.kd
    .uniform_work_group_size: 1
    .uses_dynamic_stack: false
    .vgpr_count:     256
    .vgpr_spill_count: 0
    .wavefront_size: 64
